# v36 with the instruction stream shifted by 96 bytes (24 s_nop at entry): same 64-byte phase as the 32-byte shift
# baseline (speedup 1.0000x reference)
_Z3fwd4Args:
	s_nop 0
	s_nop 0
	s_nop 0
	s_nop 0
	s_nop 0
	s_nop 0
	s_nop 0
	s_nop 0
	s_nop 0
	s_nop 0
	s_nop 0
	s_nop 0
	s_nop 0
	s_nop 0
	s_nop 0
	s_nop 0
	s_nop 0
	s_nop 0
	s_nop 0
	s_nop 0
	s_nop 0
	s_nop 0
	s_nop 0
	s_nop 0
	s_load_dword s72, s[0:1], 0xe8
	s_load_dwordx2 s[8:9], s[0:1], 0xe0
	s_load_dwordx8 s[64:71], s[0:1], 0xc0
	s_mov_b32 s96, s2
	s_add_u32 s2, s0, 0xe8
	s_addc_u32 s3, s1, 0
	v_readfirstlane_b32 s10, v0
	v_writelane_b32 v255, s2, 0
	s_mov_b32 s97, 0
	v_cmp_eq_u32_e32 vcc, 0, v0
	v_writelane_b32 v255, s3, 1
	s_waitcnt lgkmcnt(0)
	s_sub_i32 s2, s9, s8
	s_cmp_lt_i32 s2, 2
	s_cbranch_scc1 .LBB0_5
	s_getreg_b32 s2, hwreg(HW_REG_XCC_ID, 0, 4)
	s_and_b32 s97, s2, 15
	s_and_saveexec_b64 s[2:3], vcc
	s_cbranch_execz .LBB0_4
	s_mov_b64 s[4:5], exec
	v_mbcnt_lo_u32_b32 v1, s4, 0
	v_mbcnt_hi_u32_b32 v1, s5, v1
	v_cmp_eq_u32_e32 vcc, 0, v1
	s_and_b64 s[6:7], exec, vcc
	s_mov_b64 exec, s[6:7]
	s_cbranch_execz .LBB0_4
	s_lshl_b32 s6, s97, 8
	s_bcnt1_i32_b64 s4, s[4:5]
	v_mov_b32_e32 v1, s6
	v_mov_b32_e32 v2, s4
	global_atomic_add v1, v2, s[70:71] offset:1024
